# v25_trim
# baseline (speedup 1.0000x reference)
.Lp1_fast_1:
	s_add_i32 s84, s84, 1
	v_add_u32_e32 v162, 0x1100, v162
	v_add_u32_e32 v161, 0x1140, v161
	s_cmp_lg_u32 s56, 4
	v_add_u32_e32 v160, 0x1140, v160
	s_cbranch_scc0 .LBB1_125
	s_mov_b32 s59, s56
	s_lshl_b32 s96, s59, 4
	v_or_b32_e32 v164, s96, v131
	v_lshlrev_b32_e32 v163, 2, v164
	v_or_b32_e32 v66, s96, v130
	v_mul_u32_u24_e32 v165, s95, v66
	v_accvgpr_read_b32 v66, a0
	v_accvgpr_read_b32 v67, a1
	v_accvgpr_read_b32 v68, a2
	v_accvgpr_read_b32 v69, a3
.Lp1_go_1:
	v_accvgpr_write_b32 a4, v137
	v_accvgpr_write_b32 a5, v138
	v_accvgpr_write_b32 a6, v139
	v_readlane_b32 s54, v66, 0
	v_accvgpr_write_b32 a7, v140
	v_cndmask_b32_e64 v72, 0, v66, s[6:7]
	v_rcp_f32_e64 v73, -s54
	v_writelane_b32 v166, s54, 0
	v_mul_f32_e32 v70, v72, v73
	s_nop 1
	v_mfma_f32_16x16x4_f32 v[66:69], v70, v66, v[66:69]
	v_mfma_f32_16x16x4_f32 a[4:7], v70, v137, a[4:7]
	s_nop 8
	v_readlane_b32 s54, v67, 1
	v_cndmask_b32_e64 v72, 0, v67, s[8:9]
	s_nop 0
	v_rcp_f32_e64 v73, -s54
	v_writelane_b32 v166, s54, 1
	v_mul_f32_e32 v71, v72, v73
	s_nop 1
	v_mfma_f32_16x16x4_f32 v[66:69], v71, v67, v[66:69]
	v_mfma_f32_16x16x4_f32 a[4:7], v71, a5, a[4:7]
	s_nop 8
	v_readlane_b32 s54, v68, 2
	v_cndmask_b32_e64 v72, 0, v68, s[10:11]
	s_nop 0
	v_rcp_f32_e64 v73, -s54
	v_writelane_b32 v166, s54, 2
	v_mul_f32_e32 v70, v72, v73
	s_nop 1
	v_mfma_f32_16x16x4_f32 v[66:69], v70, v68, v[66:69]
	v_mfma_f32_16x16x4_f32 a[4:7], v70, a6, a[4:7]
	s_nop 8
	v_readlane_b32 s54, v69, 3
	v_cndmask_b32_e64 v72, 0, v69, s[12:13]
	s_nop 0
	v_rcp_f32_e64 v73, -s54
	v_writelane_b32 v166, s54, 3
	v_mul_f32_e32 v71, v72, v73
	s_nop 1
	v_mfma_f32_16x16x4_f32 v[66:69], v71, v69, v[66:69]
	v_mfma_f32_16x16x4_f32 a[4:7], v71, a7, a[4:7]
	s_nop 8
	v_readlane_b32 s54, v66, 20
	v_cndmask_b32_e64 v72, 0, v66, s[14:15]
	s_nop 0
	v_rcp_f32_e64 v73, -s54
	v_writelane_b32 v166, s54, 4
	v_mul_f32_e32 v70, v72, v73
	s_nop 1
	v_mfma_f32_16x16x4_f32 v[66:69], v70, v66, v[66:69]
	v_mfma_f32_16x16x4_f32 a[4:7], v70, a4, a[4:7]
	s_nop 8
	v_readlane_b32 s54, v67, 21
	v_cndmask_b32_e64 v72, 0, v67, s[16:17]
	s_nop 0
	v_rcp_f32_e64 v73, -s54
	v_writelane_b32 v166, s54, 5
	v_mul_f32_e32 v71, v72, v73
	s_nop 1
	v_mfma_f32_16x16x4_f32 v[66:69], v71, v67, v[66:69]
	v_mfma_f32_16x16x4_f32 a[4:7], v71, a5, a[4:7]
	s_nop 8
	v_readlane_b32 s54, v68, 22
	v_cndmask_b32_e64 v72, 0, v68, s[18:19]
	s_nop 0
	v_rcp_f32_e64 v73, -s54
	v_writelane_b32 v166, s54, 6
	v_mul_f32_e32 v70, v72, v73
	s_nop 1
	v_mfma_f32_16x16x4_f32 v[66:69], v70, v68, v[66:69]
	v_mfma_f32_16x16x4_f32 a[4:7], v70, a6, a[4:7]
	s_nop 8
	v_readlane_b32 s54, v69, 23
	v_cndmask_b32_e64 v72, 0, v69, s[20:21]
	s_nop 0
	v_rcp_f32_e64 v73, -s54
	v_writelane_b32 v166, s54, 7
	v_mul_f32_e32 v71, v72, v73
	s_nop 1
	v_mfma_f32_16x16x4_f32 v[66:69], v71, v69, v[66:69]
	v_mfma_f32_16x16x4_f32 a[4:7], v71, a7, a[4:7]
	s_nop 8
	v_readlane_b32 s54, v66, 40
	v_cndmask_b32_e64 v72, 0, v66, s[22:23]
	s_nop 0
	v_rcp_f32_e64 v73, -s54
	v_writelane_b32 v166, s54, 8
	v_mul_f32_e32 v70, v72, v73
	s_nop 1
	v_mfma_f32_16x16x4_f32 v[66:69], v70, v66, v[66:69]
	v_mfma_f32_16x16x4_f32 a[4:7], v70, a4, a[4:7]
	s_nop 8
	v_readlane_b32 s54, v67, 41
	v_cndmask_b32_e64 v72, 0, v67, s[24:25]
	s_nop 0
	v_rcp_f32_e64 v73, -s54
	v_writelane_b32 v166, s54, 9
	v_mul_f32_e32 v71, v72, v73
	s_nop 1
	v_mfma_f32_16x16x4_f32 v[66:69], v71, v67, v[66:69]
	v_mfma_f32_16x16x4_f32 a[4:7], v71, a5, a[4:7]
	s_nop 8
	v_readlane_b32 s54, v68, 42
	v_cndmask_b32_e64 v72, 0, v68, s[26:27]
	s_nop 0
	v_rcp_f32_e64 v73, -s54
	v_writelane_b32 v166, s54, 10
	v_mul_f32_e32 v70, v72, v73
	s_nop 1
	v_mfma_f32_16x16x4_f32 v[66:69], v70, v68, v[66:69]
	v_mfma_f32_16x16x4_f32 a[4:7], v70, a6, a[4:7]
	s_nop 8
	v_readlane_b32 s54, v69, 43
	v_cndmask_b32_e64 v72, 0, v69, s[28:29]
	s_nop 0
	v_rcp_f32_e64 v73, -s54
	v_writelane_b32 v166, s54, 11
	v_mul_f32_e32 v71, v72, v73
	s_nop 1
	v_mfma_f32_16x16x4_f32 v[66:69], v71, v69, v[66:69]
	v_mfma_f32_16x16x4_f32 a[4:7], v71, a7, a[4:7]
	s_nop 8
	v_readlane_b32 s54, v66, 60
	v_cndmask_b32_e64 v72, 0, v66, s[30:31]
	s_nop 0
	v_rcp_f32_e64 v73, -s54
	v_writelane_b32 v166, s54, 12
	v_mul_f32_e32 v70, v72, v73
	s_nop 1
	v_mfma_f32_16x16x4_f32 v[66:69], v70, v66, v[66:69]
	v_mfma_f32_16x16x4_f32 a[4:7], v70, a4, a[4:7]
	s_nop 8
	v_readlane_b32 s54, v67, 61
	v_cndmask_b32_e64 v72, 0, v67, s[34:35]
	s_nop 0
	v_rcp_f32_e64 v73, -s54
	v_writelane_b32 v166, s54, 13
	v_mul_f32_e32 v71, v72, v73
	s_nop 1
	v_mfma_f32_16x16x4_f32 v[66:69], v71, v67, v[66:69]
	v_mfma_f32_16x16x4_f32 a[4:7], v71, a5, a[4:7]
	s_nop 8
	v_readlane_b32 s54, v68, 62
	v_cndmask_b32_e64 v72, 0, v68, s[36:37]
	s_nop 0
	v_rcp_f32_e64 v73, -s54
	v_writelane_b32 v166, s54, 14
	v_mul_f32_e32 v70, v72, v73
	s_nop 1
	v_mfma_f32_16x16x4_f32 v[66:69], v70, v68, v[66:69]
	v_mfma_f32_16x16x4_f32 a[4:7], v70, a6, a[4:7]
	s_nop 8
	v_readlane_b32 s54, v69, 63
	s_nop 1
	v_writelane_b32 v166, s54, 15
	v_accvgpr_read_b32 v73, a7
	v_accvgpr_read_b32 v72, a6
	v_accvgpr_read_b32 v71, a5
	v_accvgpr_read_b32 v70, a4
	s_and_saveexec_b64 s[54:55], s[4:5]
	s_cbranch_execz .LBB1_113
	s_waitcnt lgkmcnt(2)
	v_lshl_add_u32 v167, s96, 2, v134
	ds_write_b32 v167, v166

.Lp1_fast_2:
	s_add_i32 s94, s94, 1
	v_add_u32_e32 v145, 0x1100, v145
	v_add_u32_e32 v147, 0x1140, v147
	s_cmp_lg_u32 s56, 4
	v_add_u32_e32 v11, 0x1140, v11
	s_cbranch_scc0 .LBB1_246
	s_mov_b32 s59, s56
	s_lshl_b32 s97, s59, 4
	v_or_b32_e32 v14, s97, v131
	v_lshlrev_b32_e32 v13, 2, v14
	v_or_b32_e32 v2, s97, v130
	v_mul_u32_u24_e32 v15, s57, v2
	v_accvgpr_read_b32 v2, a0
	v_accvgpr_read_b32 v3, a1
	v_accvgpr_read_b32 v4, a2
	v_accvgpr_read_b32 v5, a3
.Lp1_go_2:
	v_accvgpr_write_b32 a4, v137
	v_accvgpr_write_b32 a5, v138
	v_accvgpr_write_b32 a6, v139
	v_readlane_b32 s52, v2, 0
	v_accvgpr_write_b32 a7, v140
	v_cndmask_b32_e64 v8, 0, v2, s[6:7]
	v_rcp_f32_e64 v9, -s52
	v_writelane_b32 v16, s52, 0
	v_mul_f32_e32 v6, v8, v9
	s_nop 1
	v_mfma_f32_16x16x4_f32 v[2:5], v6, v2, v[2:5]
	v_mfma_f32_16x16x4_f32 a[4:7], v6, v137, a[4:7]
	s_nop 8
	v_readlane_b32 s52, v3, 1
	v_cndmask_b32_e64 v8, 0, v3, s[8:9]
	s_nop 0
	v_rcp_f32_e64 v9, -s52
	v_writelane_b32 v16, s52, 1
	v_mul_f32_e32 v7, v8, v9
	s_nop 1
	v_mfma_f32_16x16x4_f32 v[2:5], v7, v3, v[2:5]
	v_mfma_f32_16x16x4_f32 a[4:7], v7, a5, a[4:7]
	s_nop 8
	v_readlane_b32 s52, v4, 2
	v_cndmask_b32_e64 v8, 0, v4, s[10:11]
	s_nop 0
	v_rcp_f32_e64 v9, -s52
	v_writelane_b32 v16, s52, 2
	v_mul_f32_e32 v6, v8, v9
	s_nop 1
	v_mfma_f32_16x16x4_f32 v[2:5], v6, v4, v[2:5]
	v_mfma_f32_16x16x4_f32 a[4:7], v6, a6, a[4:7]
	s_nop 8
	v_readlane_b32 s52, v5, 3
	v_cndmask_b32_e64 v8, 0, v5, s[12:13]
	s_nop 0
	v_rcp_f32_e64 v9, -s52
	v_writelane_b32 v16, s52, 3
	v_mul_f32_e32 v7, v8, v9
	s_nop 1
	v_mfma_f32_16x16x4_f32 v[2:5], v7, v5, v[2:5]
	v_mfma_f32_16x16x4_f32 a[4:7], v7, a7, a[4:7]
	s_nop 8
	v_readlane_b32 s52, v2, 20
	v_cndmask_b32_e64 v8, 0, v2, s[14:15]
	s_nop 0
	v_rcp_f32_e64 v9, -s52
	v_writelane_b32 v16, s52, 4
	v_mul_f32_e32 v6, v8, v9
	s_nop 1
	v_mfma_f32_16x16x4_f32 v[2:5], v6, v2, v[2:5]
	v_mfma_f32_16x16x4_f32 a[4:7], v6, a4, a[4:7]
	s_nop 8
	v_readlane_b32 s52, v3, 21
	v_cndmask_b32_e64 v8, 0, v3, s[16:17]
	s_nop 0
	v_rcp_f32_e64 v9, -s52
	v_writelane_b32 v16, s52, 5
	v_mul_f32_e32 v7, v8, v9
	s_nop 1
	v_mfma_f32_16x16x4_f32 v[2:5], v7, v3, v[2:5]
	v_mfma_f32_16x16x4_f32 a[4:7], v7, a5, a[4:7]
	s_nop 8
	v_readlane_b32 s52, v4, 22
	v_cndmask_b32_e64 v8, 0, v4, s[18:19]
	s_nop 0
	v_rcp_f32_e64 v9, -s52
	v_writelane_b32 v16, s52, 6
	v_mul_f32_e32 v6, v8, v9
	s_nop 1
	v_mfma_f32_16x16x4_f32 v[2:5], v6, v4, v[2:5]
	v_mfma_f32_16x16x4_f32 a[4:7], v6, a6, a[4:7]
	s_nop 8
	v_readlane_b32 s52, v5, 23
	v_cndmask_b32_e64 v8, 0, v5, s[20:21]
	s_nop 0
	v_rcp_f32_e64 v9, -s52
	v_writelane_b32 v16, s52, 7
	v_mul_f32_e32 v7, v8, v9
	s_nop 1
	v_mfma_f32_16x16x4_f32 v[2:5], v7, v5, v[2:5]
	v_mfma_f32_16x16x4_f32 a[4:7], v7, a7, a[4:7]
	s_nop 8
	v_readlane_b32 s52, v2, 40
	v_cndmask_b32_e64 v8, 0, v2, s[22:23]
	s_nop 0
	v_rcp_f32_e64 v9, -s52
	v_writelane_b32 v16, s52, 8
	v_mul_f32_e32 v6, v8, v9
	s_nop 1
	v_mfma_f32_16x16x4_f32 v[2:5], v6, v2, v[2:5]
	v_mfma_f32_16x16x4_f32 a[4:7], v6, a4, a[4:7]
	s_nop 8
	v_readlane_b32 s52, v3, 41
	v_cndmask_b32_e64 v8, 0, v3, s[24:25]
	s_nop 0
	v_rcp_f32_e64 v9, -s52
	v_writelane_b32 v16, s52, 9
	v_mul_f32_e32 v7, v8, v9
	s_nop 1
	v_mfma_f32_16x16x4_f32 v[2:5], v7, v3, v[2:5]
	v_mfma_f32_16x16x4_f32 a[4:7], v7, a5, a[4:7]
	s_nop 8
	v_readlane_b32 s52, v4, 42
	v_cndmask_b32_e64 v8, 0, v4, s[26:27]
	s_nop 0
	v_rcp_f32_e64 v9, -s52
	v_writelane_b32 v16, s52, 10
	v_mul_f32_e32 v6, v8, v9
	s_nop 1
	v_mfma_f32_16x16x4_f32 v[2:5], v6, v4, v[2:5]
	v_mfma_f32_16x16x4_f32 a[4:7], v6, a6, a[4:7]
	s_nop 8
	v_readlane_b32 s52, v5, 43
	v_cndmask_b32_e64 v8, 0, v5, s[28:29]
	s_nop 0
	v_rcp_f32_e64 v9, -s52
	v_writelane_b32 v16, s52, 11
	v_mul_f32_e32 v7, v8, v9
	s_nop 1
	v_mfma_f32_16x16x4_f32 v[2:5], v7, v5, v[2:5]
	v_mfma_f32_16x16x4_f32 a[4:7], v7, a7, a[4:7]
	s_nop 8
	v_readlane_b32 s52, v2, 60
	v_cndmask_b32_e64 v8, 0, v2, s[30:31]
	s_nop 0
	v_rcp_f32_e64 v9, -s52
	v_writelane_b32 v16, s52, 12
	v_mul_f32_e32 v6, v8, v9
	s_nop 1
	v_mfma_f32_16x16x4_f32 v[2:5], v6, v2, v[2:5]
	v_mfma_f32_16x16x4_f32 a[4:7], v6, a4, a[4:7]
	s_nop 8
	v_readlane_b32 s52, v3, 61
	v_cndmask_b32_e64 v8, 0, v3, s[34:35]
	s_nop 0
	v_rcp_f32_e64 v9, -s52
	v_writelane_b32 v16, s52, 13
	v_mul_f32_e32 v7, v8, v9
	s_nop 1
	v_mfma_f32_16x16x4_f32 v[2:5], v7, v3, v[2:5]
	v_mfma_f32_16x16x4_f32 a[4:7], v7, a5, a[4:7]
	s_nop 8
	v_readlane_b32 s52, v4, 62
	v_cndmask_b32_e64 v8, 0, v4, s[36:37]
	s_nop 0
	v_rcp_f32_e64 v9, -s52
	v_writelane_b32 v16, s52, 14
	v_mul_f32_e32 v6, v8, v9
	s_nop 1
	v_mfma_f32_16x16x4_f32 v[2:5], v6, v4, v[2:5]
	v_mfma_f32_16x16x4_f32 a[4:7], v6, a6, a[4:7]
	s_nop 8
	v_readlane_b32 s52, v5, 63
	s_nop 1
	v_writelane_b32 v16, s52, 15
	v_accvgpr_read_b32 v9, a7
	v_accvgpr_read_b32 v8, a6
	v_accvgpr_read_b32 v7, a5
	v_accvgpr_read_b32 v6, a4
	s_and_saveexec_b64 s[52:53], s[4:5]
	s_cbranch_execz .LBB1_234
	s_waitcnt lgkmcnt(2)
	v_lshl_add_u32 v17, s97, 2, v134
	ds_write_b32 v17, v16

.Lp1_fast_3:
	s_add_i32 s68, s68, 1
	v_add_u32_e32 v40, 0x1100, v40
	v_add_u32_e32 v39, 0x1140, v39
	s_cmp_lg_u32 s52, 4
	v_add_u32_e32 v38, 0x1140, v38
	s_cbranch_scc0 .LBB1_316
	s_mov_b32 s79, s52
	s_lshl_b32 s80, s79, 4
	v_or_b32_e32 v42, s80, v19
	v_lshlrev_b32_e32 v41, 2, v42
	v_or_b32_e32 v2, s80, v18
	v_mul_u32_u24_e32 v44, s78, v2
	v_accvgpr_read_b32 v2, a0
	v_accvgpr_read_b32 v3, a1
	v_accvgpr_read_b32 v4, a2
	v_accvgpr_read_b32 v5, a3
.Lp1_go_3:
	v_accvgpr_write_b32 a4, v22
	v_accvgpr_write_b32 a5, v23
	v_accvgpr_write_b32 a6, v24
	v_readlane_b32 s52, v2, 0
	v_accvgpr_write_b32 a7, v25
	v_cndmask_b32_e64 v8, 0, v2, s[4:5]
	v_rcp_f32_e64 v9, -s52
	v_writelane_b32 v53, s52, 0
	v_mul_f32_e32 v6, v8, v9
	s_nop 1
	v_mfma_f32_16x16x4_f32 v[2:5], v6, v2, v[2:5]
	v_mfma_f32_16x16x4_f32 a[4:7], v6, v22, a[4:7]
	s_nop 8
	v_readlane_b32 s52, v3, 1
	v_cndmask_b32_e64 v8, 0, v3, s[6:7]
	s_nop 0
	v_rcp_f32_e64 v9, -s52
	v_writelane_b32 v53, s52, 1
	v_mul_f32_e32 v7, v8, v9
	s_nop 1
	v_mfma_f32_16x16x4_f32 v[2:5], v7, v3, v[2:5]
	v_mfma_f32_16x16x4_f32 a[4:7], v7, a5, a[4:7]
	s_nop 8
	v_readlane_b32 s52, v4, 2
	v_cndmask_b32_e64 v8, 0, v4, s[8:9]
	s_nop 0
	v_rcp_f32_e64 v9, -s52
	v_writelane_b32 v53, s52, 2
	v_mul_f32_e32 v6, v8, v9
	s_nop 1
	v_mfma_f32_16x16x4_f32 v[2:5], v6, v4, v[2:5]
	v_mfma_f32_16x16x4_f32 a[4:7], v6, a6, a[4:7]
	s_nop 8
	v_readlane_b32 s52, v5, 3
	v_cndmask_b32_e64 v8, 0, v5, s[10:11]
	s_nop 0
	v_rcp_f32_e64 v9, -s52
	v_writelane_b32 v53, s52, 3
	v_mul_f32_e32 v7, v8, v9
	s_nop 1
	v_mfma_f32_16x16x4_f32 v[2:5], v7, v5, v[2:5]
	v_mfma_f32_16x16x4_f32 a[4:7], v7, a7, a[4:7]
	s_nop 8
	v_readlane_b32 s52, v2, 20
	v_cndmask_b32_e64 v8, 0, v2, s[12:13]
	s_nop 0
	v_rcp_f32_e64 v9, -s52
	v_writelane_b32 v53, s52, 4
	v_mul_f32_e32 v6, v8, v9
	s_nop 1
	v_mfma_f32_16x16x4_f32 v[2:5], v6, v2, v[2:5]
	v_mfma_f32_16x16x4_f32 a[4:7], v6, a4, a[4:7]
	s_nop 8
	v_readlane_b32 s52, v3, 21
	v_cndmask_b32_e64 v8, 0, v3, s[14:15]
	s_nop 0
	v_rcp_f32_e64 v9, -s52
	v_writelane_b32 v53, s52, 5
	v_mul_f32_e32 v7, v8, v9
	s_nop 1
	v_mfma_f32_16x16x4_f32 v[2:5], v7, v3, v[2:5]
	v_mfma_f32_16x16x4_f32 a[4:7], v7, a5, a[4:7]
	s_nop 8
	v_readlane_b32 s52, v4, 22
	v_cndmask_b32_e64 v8, 0, v4, s[16:17]
	s_nop 0
	v_rcp_f32_e64 v9, -s52
	v_writelane_b32 v53, s52, 6
	v_mul_f32_e32 v6, v8, v9
	s_nop 1
	v_mfma_f32_16x16x4_f32 v[2:5], v6, v4, v[2:5]
	v_mfma_f32_16x16x4_f32 a[4:7], v6, a6, a[4:7]
	s_nop 8
	v_readlane_b32 s52, v5, 23
	v_cndmask_b32_e64 v8, 0, v5, s[18:19]
	s_nop 0
	v_rcp_f32_e64 v9, -s52
	v_writelane_b32 v53, s52, 7
	v_mul_f32_e32 v7, v8, v9
	s_nop 1
	v_mfma_f32_16x16x4_f32 v[2:5], v7, v5, v[2:5]
	v_mfma_f32_16x16x4_f32 a[4:7], v7, a7, a[4:7]
	s_nop 8
	v_readlane_b32 s52, v2, 40
	v_cndmask_b32_e64 v8, 0, v2, s[20:21]
	s_nop 0
	v_rcp_f32_e64 v9, -s52
	v_writelane_b32 v53, s52, 8
	v_mul_f32_e32 v6, v8, v9
	s_nop 1
	v_mfma_f32_16x16x4_f32 v[2:5], v6, v2, v[2:5]
	v_mfma_f32_16x16x4_f32 a[4:7], v6, a4, a[4:7]
	s_nop 8
	v_readlane_b32 s52, v3, 41
	v_cndmask_b32_e64 v8, 0, v3, s[22:23]
	s_nop 0
	v_rcp_f32_e64 v9, -s52
	v_writelane_b32 v53, s52, 9
	v_mul_f32_e32 v7, v8, v9
	s_nop 1
	v_mfma_f32_16x16x4_f32 v[2:5], v7, v3, v[2:5]
	v_mfma_f32_16x16x4_f32 a[4:7], v7, a5, a[4:7]
	s_nop 8
	v_readlane_b32 s52, v4, 42
	v_cndmask_b32_e64 v8, 0, v4, s[24:25]
	s_nop 0
	v_rcp_f32_e64 v9, -s52
	v_writelane_b32 v53, s52, 10
	v_mul_f32_e32 v6, v8, v9
	s_nop 1
	v_mfma_f32_16x16x4_f32 v[2:5], v6, v4, v[2:5]
	v_mfma_f32_16x16x4_f32 a[4:7], v6, a6, a[4:7]
	s_nop 8
	v_readlane_b32 s52, v5, 43
	v_cndmask_b32_e64 v8, 0, v5, s[26:27]
	s_nop 0
	v_rcp_f32_e64 v9, -s52
	v_writelane_b32 v53, s52, 11
	v_mul_f32_e32 v7, v8, v9
	s_nop 1
	v_mfma_f32_16x16x4_f32 v[2:5], v7, v5, v[2:5]
	v_mfma_f32_16x16x4_f32 a[4:7], v7, a7, a[4:7]
	s_nop 8
	v_readlane_b32 s52, v2, 60
	v_cndmask_b32_e64 v8, 0, v2, s[28:29]
	s_nop 0
	v_rcp_f32_e64 v9, -s52
	v_writelane_b32 v53, s52, 12
	v_mul_f32_e32 v6, v8, v9
	s_nop 1
	v_mfma_f32_16x16x4_f32 v[2:5], v6, v2, v[2:5]
	v_mfma_f32_16x16x4_f32 a[4:7], v6, a4, a[4:7]
	s_nop 8
	v_readlane_b32 s52, v3, 61
	v_cndmask_b32_e64 v8, 0, v3, s[30:31]
	s_nop 0
	v_rcp_f32_e64 v9, -s52
	v_writelane_b32 v53, s52, 13
	v_mul_f32_e32 v7, v8, v9
	s_nop 1
	v_mfma_f32_16x16x4_f32 v[2:5], v7, v3, v[2:5]
	v_mfma_f32_16x16x4_f32 a[4:7], v7, a5, a[4:7]
	s_nop 8
	v_readlane_b32 s52, v4, 62
	v_cndmask_b32_e64 v8, 0, v4, s[34:35]
	s_nop 0
	v_rcp_f32_e64 v9, -s52
	v_writelane_b32 v53, s52, 14
	v_mul_f32_e32 v6, v8, v9
	s_nop 1
	v_mfma_f32_16x16x4_f32 v[2:5], v6, v4, v[2:5]
	v_mfma_f32_16x16x4_f32 a[4:7], v6, a6, a[4:7]
	s_nop 8
	v_readlane_b32 s52, v5, 63
	s_nop 1
	v_writelane_b32 v53, s52, 15
	v_accvgpr_read_b32 v9, a7
	v_accvgpr_read_b32 v8, a6
	v_accvgpr_read_b32 v7, a5
	v_accvgpr_read_b32 v6, a4
	s_and_saveexec_b64 s[52:53], s[2:3]
	s_cbranch_execz .LBB1_304
	s_waitcnt lgkmcnt(2)
	v_lshl_add_u32 v54, s80, 2, v11
	ds_write_b32 v54, v53

.Lp1_fast_4:
	s_add_i32 s65, s65, 1
	v_add_u32_e32 v30, 0x1100, v30
	v_add_u32_e32 v32, 0x1140, v32
	s_cmp_lg_u32 s52, 4
	v_add_u32_e32 v12, 0x1140, v12
	s_cbranch_scc0 .LBB1_357
	s_mov_b32 s74, s52
	s_lshl_b32 s75, s74, 4
	v_or_b32_e32 v34, s75, v19
	v_lshlrev_b32_e32 v14, 2, v34
	v_or_b32_e32 v0, s75, v18
	v_mul_u32_u24_e32 v35, s64, v0
	v_accvgpr_read_b32 v0, a0
	v_accvgpr_read_b32 v1, a1
	v_accvgpr_read_b32 v2, a2
	v_accvgpr_read_b32 v3, a3
.Lp1_go_4:
	v_accvgpr_write_b32 a4, v22
	v_accvgpr_write_b32 a5, v23
	v_accvgpr_write_b32 a6, v24
	v_readlane_b32 s52, v0, 0
	v_accvgpr_write_b32 a7, v25
	v_cndmask_b32_e64 v6, 0, v0, s[4:5]
	v_rcp_f32_e64 v7, -s52
	v_writelane_b32 v36, s52, 0
	v_mul_f32_e32 v4, v6, v7
	s_nop 1
	v_mfma_f32_16x16x4_f32 v[0:3], v4, v0, v[0:3]
	v_mfma_f32_16x16x4_f32 a[4:7], v4, v22, a[4:7]
	s_nop 8
	v_readlane_b32 s52, v1, 1
	v_cndmask_b32_e64 v6, 0, v1, s[6:7]
	s_nop 0
	v_rcp_f32_e64 v7, -s52
	v_writelane_b32 v36, s52, 1
	v_mul_f32_e32 v5, v6, v7
	s_nop 1
	v_mfma_f32_16x16x4_f32 v[0:3], v5, v1, v[0:3]
	v_mfma_f32_16x16x4_f32 a[4:7], v5, a5, a[4:7]
	s_nop 8
	v_readlane_b32 s52, v2, 2
	v_cndmask_b32_e64 v6, 0, v2, s[8:9]
	s_nop 0
	v_rcp_f32_e64 v7, -s52
	v_writelane_b32 v36, s52, 2
	v_mul_f32_e32 v4, v6, v7
	s_nop 1
	v_mfma_f32_16x16x4_f32 v[0:3], v4, v2, v[0:3]
	v_mfma_f32_16x16x4_f32 a[4:7], v4, a6, a[4:7]
	s_nop 8
	v_readlane_b32 s52, v3, 3
	v_cndmask_b32_e64 v6, 0, v3, s[10:11]
	s_nop 0
	v_rcp_f32_e64 v7, -s52
	v_writelane_b32 v36, s52, 3
	v_mul_f32_e32 v5, v6, v7
	s_nop 1
	v_mfma_f32_16x16x4_f32 v[0:3], v5, v3, v[0:3]
	v_mfma_f32_16x16x4_f32 a[4:7], v5, a7, a[4:7]
	s_nop 8
	v_readlane_b32 s52, v0, 20
	v_cndmask_b32_e64 v6, 0, v0, s[12:13]
	s_nop 0
	v_rcp_f32_e64 v7, -s52
	v_writelane_b32 v36, s52, 4
	v_mul_f32_e32 v4, v6, v7
	s_nop 1
	v_mfma_f32_16x16x4_f32 v[0:3], v4, v0, v[0:3]
	v_mfma_f32_16x16x4_f32 a[4:7], v4, a4, a[4:7]
	s_nop 8
	v_readlane_b32 s52, v1, 21
	v_cndmask_b32_e64 v6, 0, v1, s[14:15]
	s_nop 0
	v_rcp_f32_e64 v7, -s52
	v_writelane_b32 v36, s52, 5
	v_mul_f32_e32 v5, v6, v7
	s_nop 1
	v_mfma_f32_16x16x4_f32 v[0:3], v5, v1, v[0:3]
	v_mfma_f32_16x16x4_f32 a[4:7], v5, a5, a[4:7]
	s_nop 8
	v_readlane_b32 s52, v2, 22
	v_cndmask_b32_e64 v6, 0, v2, s[16:17]
	s_nop 0
	v_rcp_f32_e64 v7, -s52
	v_writelane_b32 v36, s52, 6
	v_mul_f32_e32 v4, v6, v7
	s_nop 1
	v_mfma_f32_16x16x4_f32 v[0:3], v4, v2, v[0:3]
	v_mfma_f32_16x16x4_f32 a[4:7], v4, a6, a[4:7]
	s_nop 8
	v_readlane_b32 s52, v3, 23
	v_cndmask_b32_e64 v6, 0, v3, s[18:19]
	s_nop 0
	v_rcp_f32_e64 v7, -s52
	v_writelane_b32 v36, s52, 7
	v_mul_f32_e32 v5, v6, v7
	s_nop 1
	v_mfma_f32_16x16x4_f32 v[0:3], v5, v3, v[0:3]
	v_mfma_f32_16x16x4_f32 a[4:7], v5, a7, a[4:7]
	s_nop 8
	v_readlane_b32 s52, v0, 40
	v_cndmask_b32_e64 v6, 0, v0, s[20:21]
	s_nop 0
	v_rcp_f32_e64 v7, -s52
	v_writelane_b32 v36, s52, 8
	v_mul_f32_e32 v4, v6, v7
	s_nop 1
	v_mfma_f32_16x16x4_f32 v[0:3], v4, v0, v[0:3]
	v_mfma_f32_16x16x4_f32 a[4:7], v4, a4, a[4:7]
	s_nop 8
	v_readlane_b32 s52, v1, 41
	v_cndmask_b32_e64 v6, 0, v1, s[22:23]
	s_nop 0
	v_rcp_f32_e64 v7, -s52
	v_writelane_b32 v36, s52, 9
	v_mul_f32_e32 v5, v6, v7
	s_nop 1
	v_mfma_f32_16x16x4_f32 v[0:3], v5, v1, v[0:3]
	v_mfma_f32_16x16x4_f32 a[4:7], v5, a5, a[4:7]
	s_nop 8
	v_readlane_b32 s52, v2, 42
	v_cndmask_b32_e64 v6, 0, v2, s[24:25]
	s_nop 0
	v_rcp_f32_e64 v7, -s52
	v_writelane_b32 v36, s52, 10
	v_mul_f32_e32 v4, v6, v7
	s_nop 1
	v_mfma_f32_16x16x4_f32 v[0:3], v4, v2, v[0:3]
	v_mfma_f32_16x16x4_f32 a[4:7], v4, a6, a[4:7]
	s_nop 8
	v_readlane_b32 s52, v3, 43
	v_cndmask_b32_e64 v6, 0, v3, s[26:27]
	s_nop 0
	v_rcp_f32_e64 v7, -s52
	v_writelane_b32 v36, s52, 11
	v_mul_f32_e32 v5, v6, v7
	s_nop 1
	v_mfma_f32_16x16x4_f32 v[0:3], v5, v3, v[0:3]
	v_mfma_f32_16x16x4_f32 a[4:7], v5, a7, a[4:7]
	s_nop 8
	v_readlane_b32 s52, v0, 60
	v_cndmask_b32_e64 v6, 0, v0, s[28:29]
	s_nop 0
	v_rcp_f32_e64 v7, -s52
	v_writelane_b32 v36, s52, 12
	v_mul_f32_e32 v4, v6, v7
	s_nop 1
	v_mfma_f32_16x16x4_f32 v[0:3], v4, v0, v[0:3]
	v_mfma_f32_16x16x4_f32 a[4:7], v4, a4, a[4:7]
	s_nop 8
	v_readlane_b32 s52, v1, 61
	v_cndmask_b32_e64 v6, 0, v1, s[30:31]
	s_nop 0
	v_rcp_f32_e64 v7, -s52
	v_writelane_b32 v36, s52, 13
	v_mul_f32_e32 v5, v6, v7
	s_nop 1
	v_mfma_f32_16x16x4_f32 v[0:3], v5, v1, v[0:3]
	v_mfma_f32_16x16x4_f32 a[4:7], v5, a5, a[4:7]
	s_nop 8
	v_readlane_b32 s52, v2, 62
	v_cndmask_b32_e64 v6, 0, v2, s[34:35]
	s_nop 0
	v_rcp_f32_e64 v7, -s52
	v_writelane_b32 v36, s52, 14
	v_mul_f32_e32 v4, v6, v7
	s_nop 1
	v_mfma_f32_16x16x4_f32 v[0:3], v4, v2, v[0:3]
	v_mfma_f32_16x16x4_f32 a[4:7], v4, a6, a[4:7]
	s_nop 8
	v_readlane_b32 s52, v3, 63
	s_nop 1
	v_writelane_b32 v36, s52, 15
	v_accvgpr_read_b32 v7, a7
	v_accvgpr_read_b32 v6, a6
	v_accvgpr_read_b32 v5, a5
	v_accvgpr_read_b32 v4, a4
	s_and_saveexec_b64 s[52:53], s[2:3]
	s_cbranch_execz .LBB1_345
	s_waitcnt lgkmcnt(2)
	v_lshl_add_u32 v37, s75, 2, v11
	ds_write_b32 v37, v36
